# v8 + sc1 write-through stores in k0 prep
# speedup vs baseline: 1.0244x; 1.0244x over previous
.LBB0_6:
	s_or_b64 exec, exec, s[6:7]
	s_waitcnt vmcnt(0)
	v_cndmask_b32_e64 v1, v13, v12, s[4:5]
	v_cndmask_b32_e64 v1, v1, v11, s[10:11]
	v_cndmask_b32_e32 v1, v1, v10, vcc
	v_mul_f32_e32 v14, 0x439044fe, v1
	v_cndmask_b32_e64 v1, v7, v6, s[4:5]
	v_ashrrev_i32_e32 v19, 31, v18
	v_cndmask_b32_e64 v1, v1, v5, s[10:11]
	v_lshl_add_u64 v[2:3], v[18:19], 4, s[12:13]
	v_cndmask_b32_e32 v1, v1, v4, vcc
	v_add_co_u32_e32 v2, vcc, 0x787000, v2
	v_mul_f32_e32 v16, 0x439044fe, v1
	s_nop 0
	v_addc_co_u32_e32 v3, vcc, 0, v3, vcc
	s_mov_b64 s[4:5], 0
	global_store_dwordx4 v[2:3], v[14:17], off sc1
.LBB0_7:
	s_and_b64 vcc, exec, s[4:5]
	s_cbranch_vccz .LBB0_10
	s_load_dwordx4 s[4:7], s[0:1], 0x0
	s_lshl_b32 s8, s2, 2
	s_add_i32 s9, s8, 0xfffff000
	s_cmpk_lt_i32 s2, 0x400
	s_cselect_b64 s[0:1], -1, 0
	s_and_b64 s[2:3], s[0:1], exec
	s_waitcnt lgkmcnt(0)
	s_cselect_b32 s2, s5, s7
	v_and_b32_e32 v1, 63, v0
	v_lshrrev_b32_e32 v0, 6, v0
	v_mov_b32_e32 v3, s2
	s_cselect_b32 s2, s8, s9
	s_cselect_b32 s3, s4, s6
	v_or_b32_e32 v0, s2, v0
	s_movk_i32 s2, 0x300
	v_mov_b32_e32 v2, s3
	v_mad_i64_i32 v[14:15], s[2:3], v0, s2, 0
	v_lshl_add_u64 v[2:3], v[14:15], 2, v[2:3]
	v_lshlrev_b32_e32 v16, 4, v1
	v_mov_b32_e32 v17, 0
	v_lshl_add_u64 v[18:19], v[2:3], 0, v[16:17]
	global_load_dwordx4 v[2:5], v[18:19], off
	global_load_dwordx4 v[6:9], v[18:19], off offset:1024
	global_load_dwordx4 v[10:13], v[18:19], off offset:2048
	v_mbcnt_lo_u32_b32 v16, -1, 0
	v_mbcnt_hi_u32_b32 v16, -1, v16
	v_and_b32_e32 v19, 64, v16
	v_xor_b32_e32 v18, 16, v16
	v_add_u32_e32 v19, 64, v19
	s_cselect_b32 s2, 0, 0x600000
	v_xor_b32_e32 v20, 32, v16
	v_cmp_lt_i32_e32 vcc, v18, v19
	s_add_u32 s2, s12, s2
	s_addc_u32 s3, s13, 0
	v_cndmask_b32_e32 v18, v16, v18, vcc
	v_cmp_lt_i32_e32 vcc, v20, v19
	v_lshl_add_u64 v[14:15], v[14:15], 1, s[2:3]
	s_movk_i32 s4, 0x7fff
	v_cndmask_b32_e32 v19, v16, v20, vcc
	v_lshlrev_b32_e32 v16, 3, v1
	v_lshl_add_u64 v[14:15], v[14:15], 0, v[16:17]
	v_lshlrev_b32_e32 v18, 2, v18
	s_mov_b32 s5, 0x7060302
	v_cmp_eq_u32_e32 vcc, 0, v1
	s_waitcnt vmcnt(2)
	v_mul_f32_e32 v16, v3, v3
	v_fmac_f32_e32 v16, v2, v2
	v_fmac_f32_e32 v16, v4, v4
	v_fmac_f32_e32 v16, v5, v5
	s_waitcnt vmcnt(1)
	v_fmac_f32_e32 v16, v6, v6
	v_fmac_f32_e32 v16, v7, v7
	v_fmac_f32_e32 v16, v8, v8
	v_fmac_f32_e32 v16, v9, v9
	s_waitcnt vmcnt(0)
	v_fmac_f32_e32 v16, v10, v10
	v_fmac_f32_e32 v16, v11, v11
	v_fmac_f32_e32 v16, v12, v12
	v_bfe_u32 v20, v4, 16, 1
	v_bfe_u32 v21, v3, 16, 1
	v_fmac_f32_e32 v16, v13, v13
	v_add3_u32 v21, v3, v21, s4
	v_add3_u32 v3, v4, v20, s4
	v_add_f32_dpp v4, v16, v16 row_ror:1 row_mask:0xf bank_mask:0xf bound_ctrl:1
	v_bfe_u32 v26, v6, 16, 1
	v_bfe_u32 v22, v2, 16, 1
	v_add_f32_dpp v4, v4, v4 row_ror:2 row_mask:0xf bank_mask:0xf bound_ctrl:1
	v_bfe_u32 v25, v7, 16, 1
	v_add3_u32 v20, v6, v26, s4
	v_add_f32_dpp v4, v4, v4 row_ror:4 row_mask:0xf bank_mask:0xf bound_ctrl:1
	v_add3_u32 v2, v2, v22, s4
	v_add3_u32 v22, v7, v25, s4
	v_add_f32_dpp v6, v4, v4 row_ror:8 row_mask:0xf bank_mask:0xf bound_ctrl:1
	ds_bpermute_b32 v7, v18, v6
	v_bfe_u32 v17, v5, 16, 1
	v_bfe_u32 v23, v9, 16, 1
	v_bfe_u32 v24, v8, 16, 1
	v_add3_u32 v17, v5, v17, s4
	v_add3_u32 v24, v8, v24, s4
	v_add3_u32 v23, v9, v23, s4
	v_perm_b32 v3, v17, v3, s5
	v_perm_b32 v2, v21, v2, s5
	v_perm_b32 v5, v23, v24, s5
	v_perm_b32 v4, v22, v20, s5
	global_store_dwordx2 v[14:15], v[2:3], off sc1
	global_store_dwordx2 v[14:15], v[4:5], off offset:512 sc1
	s_waitcnt lgkmcnt(0)
	v_add_f32_e32 v2, v6, v7
	v_lshlrev_b32_e32 v3, 2, v19
	ds_bpermute_b32 v3, v3, v2
	v_bfe_u32 v27, v13, 16, 1
	v_bfe_u32 v28, v12, 16, 1
	v_bfe_u32 v29, v11, 16, 1
	v_bfe_u32 v30, v10, 16, 1
	v_add3_u32 v25, v10, v30, s4
	v_add3_u32 v26, v11, v29, s4
	v_add3_u32 v28, v12, v28, s4
	v_add3_u32 v27, v13, v27, s4
	v_perm_b32 v5, v27, v28, s5
	v_perm_b32 v4, v26, v25, s5
	global_store_dwordx2 v[14:15], v[4:5], off offset:1024 sc1
	s_and_saveexec_b64 s[2:3], vcc
	s_cbranch_execz .LBB0_10
	s_mov_b32 s2, 0x780000
	s_and_b64 s[0:1], s[0:1], exec
	s_cselect_b32 s0, s2, 0x784000
	s_add_u32 s0, s12, s0
	v_ashrrev_i32_e32 v1, 31, v0
	s_addc_u32 s1, s13, 0
	v_lshl_add_u64 v[0:1], v[0:1], 2, s[0:1]
	s_waitcnt lgkmcnt(0)
	v_add_f32_e32 v2, v2, v3
	global_store_dword v[0:1], v2, off sc1
